# baseline (speedup 1.0000x reference)
.Lop_deskew:
	s_or_b64 exec, exec, s[4:5]
	v_lshl_add_u64 v[230:231], v[136:137], 0, v[130:131]
	v_readfirstlane_b32 s9, v163
	v_lshl_add_u64 v[182:183], v[230:231], 0, s[16:17]
	s_mov_b32 m0, s9
	v_readfirstlane_b32 s9, v164
	global_load_lds_dwordx4 v[182:183], off
	v_lshl_add_u64 v[182:183], v[230:231], 0, s[18:19]
	s_mov_b32 m0, s9
	s_nop 0
	global_load_lds_dwordx4 v[182:183], off
	ds_read_b128 v[166:169], v162
	ds_read_b128 v[170:173], v162 offset:1024
	ds_read_b128 v[174:177], v162 offset:2048
	ds_read_b128 v[178:181], v162 offset:3072
	ds_read_b128 v[182:185], v141
	ds_read_b128 v[186:189], v141 offset:1024
	ds_read_b128 v[190:193], v140
	ds_read_b128 v[194:197], v140 offset:1024
	ds_read_b128 v[198:201], v139
	ds_read_b128 v[202:205], v139 offset:1024
	ds_read_b128 v[206:209], v138
	ds_read_b128 v[210:213], v138 offset:1024
	s_waitcnt lgkmcnt(0)
	ds_read_b128 v[214:217], v160
	ds_read_b128 v[218:221], v160 offset:1024
	ds_read_b128 v[222:225], v160 offset:2048
	ds_read_b128 v[226:229], v160 offset:3072
	ds_read_b128 v[34:37], v141 offset:16384
	ds_read_b128 v[38:41], v141 offset:17408
	ds_read_b128 v[42:45], v140 offset:16384
	ds_read_b128 v[46:49], v140 offset:17408
	ds_read_b128 v[50:53], v139 offset:16384
	ds_read_b128 v[54:57], v139 offset:17408
	ds_read_b128 v[58:61], v138 offset:16384
	ds_read_b128 v[62:65], v138 offset:17408
	v_mfma_f32_16x16x32_f16 v[126:129], v[182:185], v[166:169], v[126:129]
	v_mfma_f32_16x16x32_f16 v[122:125], v[182:185], v[174:177], v[122:125]
	v_mfma_f32_16x16x32_f16 v[118:121], v[190:193], v[166:169], v[118:121]
	v_mfma_f32_16x16x32_f16 v[114:117], v[190:193], v[174:177], v[114:117]
	v_mfma_f32_16x16x32_f16 v[110:113], v[198:201], v[166:169], v[110:113]
	v_mfma_f32_16x16x32_f16 v[106:109], v[198:201], v[174:177], v[106:109]
	v_mfma_f32_16x16x32_f16 v[102:105], v[206:209], v[166:169], v[102:105]
	v_mfma_f32_16x16x32_f16 v[98:101], v[206:209], v[174:177], v[98:101]
	v_mfma_f32_16x16x32_f16 v[126:129], v[186:189], v[170:173], v[126:129]
	v_mfma_f32_16x16x32_f16 v[122:125], v[186:189], v[178:181], v[122:125]
	v_mfma_f32_16x16x32_f16 v[118:121], v[194:197], v[170:173], v[118:121]
	v_mfma_f32_16x16x32_f16 v[114:117], v[194:197], v[178:181], v[114:117]
	v_mfma_f32_16x16x32_f16 v[110:113], v[202:205], v[170:173], v[110:113]
	v_mfma_f32_16x16x32_f16 v[106:109], v[202:205], v[178:181], v[106:109]
	v_mfma_f32_16x16x32_f16 v[102:105], v[210:213], v[170:173], v[102:105]
	v_mfma_f32_16x16x32_f16 v[98:101], v[210:213], v[178:181], v[98:101]
	s_waitcnt vmcnt(0)
	s_barrier
	s_waitcnt lgkmcnt(0)
	s_nop 3
	ds_read_b128 v[166:169], v151
	ds_read_b128 v[170:173], v151 offset:1024
	ds_read_b128 v[174:177], v151 offset:2048
	ds_read_b128 v[178:181], v151 offset:3072
	ds_read_b128 v[182:185], v141 offset:32768
	ds_read_b128 v[186:189], v141 offset:33792
	ds_read_b128 v[190:193], v140 offset:32768
	ds_read_b128 v[194:197], v140 offset:33792
	ds_read_b128 v[198:201], v139 offset:32768
	ds_read_b128 v[202:205], v139 offset:33792
	ds_read_b128 v[206:209], v138 offset:32768
	ds_read_b128 v[210:213], v138 offset:33792
	v_mfma_f32_16x16x32_f16 v[30:33], v[34:37], v[214:217], v[30:33]
	v_mfma_f32_16x16x32_f16 v[26:29], v[34:37], v[222:225], v[26:29]
	v_mfma_f32_16x16x32_f16 v[22:25], v[42:45], v[214:217], v[22:25]
	v_mfma_f32_16x16x32_f16 v[18:21], v[42:45], v[222:225], v[18:21]
	v_mfma_f32_16x16x32_f16 v[14:17], v[50:53], v[214:217], v[14:17]
	v_mfma_f32_16x16x32_f16 v[10:13], v[50:53], v[222:225], v[10:13]
	v_mfma_f32_16x16x32_f16 v[6:9], v[58:61], v[214:217], v[6:9]
	v_mfma_f32_16x16x32_f16 v[2:5], v[58:61], v[222:225], v[2:5]
	v_mfma_f32_16x16x32_f16 v[30:33], v[38:41], v[218:221], v[30:33]
	v_mfma_f32_16x16x32_f16 v[26:29], v[38:41], v[226:229], v[26:29]
	v_mfma_f32_16x16x32_f16 v[22:25], v[46:49], v[218:221], v[22:25]
	v_mfma_f32_16x16x32_f16 v[18:21], v[46:49], v[226:229], v[18:21]
	v_mfma_f32_16x16x32_f16 v[14:17], v[54:57], v[218:221], v[14:17]
	v_mfma_f32_16x16x32_f16 v[10:13], v[54:57], v[226:229], v[10:13]
	v_mfma_f32_16x16x32_f16 v[6:9], v[62:65], v[218:221], v[6:9]
	v_mfma_f32_16x16x32_f16 v[2:5], v[62:65], v[226:229], v[2:5]
	s_waitcnt lgkmcnt(0)
	s_nop 3
	ds_read_b128 v[214:217], v144
	ds_read_b128 v[218:221], v144 offset:1024
	ds_read_b128 v[222:225], v144 offset:2048
	ds_read_b128 v[226:229], v144 offset:3072
	ds_read_b128 v[34:37], v141 offset:49152
	ds_read_b128 v[38:41], v141 offset:50176
	ds_read_b128 v[42:45], v140 offset:49152
	ds_read_b128 v[46:49], v140 offset:50176
	ds_read_b128 v[50:53], v139 offset:49152
	ds_read_b128 v[54:57], v139 offset:50176
	ds_read_b128 v[58:61], v138 offset:49152
	ds_read_b128 v[62:65], v138 offset:50176
	v_mfma_f32_16x16x32_f16 v[126:129], v[182:185], v[166:169], v[126:129]
	v_mfma_f32_16x16x32_f16 v[122:125], v[182:185], v[174:177], v[122:125]
	v_mfma_f32_16x16x32_f16 v[118:121], v[190:193], v[166:169], v[118:121]
	v_mfma_f32_16x16x32_f16 v[114:117], v[190:193], v[174:177], v[114:117]
	v_mfma_f32_16x16x32_f16 v[110:113], v[198:201], v[166:169], v[110:113]
	v_mfma_f32_16x16x32_f16 v[106:109], v[198:201], v[174:177], v[106:109]
	v_mfma_f32_16x16x32_f16 v[102:105], v[206:209], v[166:169], v[102:105]
	v_mfma_f32_16x16x32_f16 v[98:101], v[206:209], v[174:177], v[98:101]
	v_mfma_f32_16x16x32_f16 v[126:129], v[186:189], v[170:173], v[126:129]
	v_mfma_f32_16x16x32_f16 v[122:125], v[186:189], v[178:181], v[122:125]
	v_mfma_f32_16x16x32_f16 v[118:121], v[194:197], v[170:173], v[118:121]
	v_mfma_f32_16x16x32_f16 v[114:117], v[194:197], v[178:181], v[114:117]
	v_mfma_f32_16x16x32_f16 v[110:113], v[202:205], v[170:173], v[110:113]
	v_mfma_f32_16x16x32_f16 v[106:109], v[202:205], v[178:181], v[106:109]
	v_mfma_f32_16x16x32_f16 v[102:105], v[210:213], v[170:173], v[102:105]
	v_mfma_f32_16x16x32_f16 v[98:101], v[210:213], v[178:181], v[98:101]
	s_waitcnt lgkmcnt(0)
	v_mfma_f32_16x16x32_f16 v[30:33], v[34:37], v[214:217], v[30:33]
	v_mfma_f32_16x16x32_f16 v[26:29], v[34:37], v[222:225], v[26:29]
	v_mfma_f32_16x16x32_f16 v[22:25], v[42:45], v[214:217], v[22:25]
	v_mfma_f32_16x16x32_f16 v[18:21], v[42:45], v[222:225], v[18:21]
	v_mfma_f32_16x16x32_f16 v[14:17], v[50:53], v[214:217], v[14:17]
	v_mfma_f32_16x16x32_f16 v[10:13], v[50:53], v[222:225], v[10:13]
	v_mfma_f32_16x16x32_f16 v[6:9], v[58:61], v[214:217], v[6:9]
	v_mfma_f32_16x16x32_f16 v[2:5], v[58:61], v[222:225], v[2:5]
	v_mfma_f32_16x16x32_f16 v[30:33], v[38:41], v[218:221], v[30:33]
	v_mfma_f32_16x16x32_f16 v[26:29], v[38:41], v[226:229], v[26:29]
	v_mfma_f32_16x16x32_f16 v[22:25], v[46:49], v[218:221], v[22:25]
	v_mfma_f32_16x16x32_f16 v[18:21], v[46:49], v[226:229], v[18:21]
	v_mfma_f32_16x16x32_f16 v[14:17], v[54:57], v[218:221], v[14:17]
	v_mfma_f32_16x16x32_f16 v[10:13], v[54:57], v[226:229], v[10:13]
	v_mfma_f32_16x16x32_f16 v[6:9], v[62:65], v[218:221], v[6:9]
	v_mfma_f32_16x16x32_f16 v[2:5], v[62:65], v[226:229], v[2:5]
	v_and_b32_e32 v130, 15, v0
	v_bfe_u32 v131, v0, 6, 2
	v_lshl_add_u32 v130, v131, 5, v130
	v_add_u32_e32 v130, s33, v130
	v_bfe_u32 v131, v0, 4, 2
	v_lshrrev_b32_e32 v132, 8, v0
	v_lshlrev_b32_e32 v131, 2, v131
	v_lshl_add_u32 v131, v132, 6, v131
	v_add_u32_e32 v131, s8, v131
	v_lshlrev_b32_e32 v131, 2, v131
	v_lshl_add_u32 v130, v130, 12, v131
	v_mov_b32_e32 v131, 0
	s_mov_b64 s[4:5], 0x10000
	s_waitcnt lgkmcnt(0)
	v_lshl_add_u64 v[130:131], s[36:37], 0, v[130:131]
	v_lshl_add_u64 v[132:133], v[130:131], 0, s[4:5]
	s_nop 7
	s_nop 7
	v_pk_add_f32 v[126:127], v[126:127], v[30:31]
	v_pk_add_f32 v[128:129], v[128:129], v[32:33]
	v_pk_mul_f32 v[126:127], v[126:127], s[34:35] op_sel_hi:[1,0]
	v_pk_mul_f32 v[128:129], v[128:129], s[34:35] op_sel_hi:[1,0]
	global_store_dwordx4 v[130:131], v[126:129], off nt
	v_pk_add_f32 v[122:123], v[122:123], v[26:27]
	v_pk_add_f32 v[124:125], v[124:125], v[28:29]
	v_pk_mul_f32 v[122:123], v[122:123], s[34:35] op_sel_hi:[1,0]
	v_pk_mul_f32 v[124:125], v[124:125], s[34:35] op_sel_hi:[1,0]
	global_store_dwordx4 v[132:133], v[122:125], off nt
	v_pk_add_f32 v[118:119], v[118:119], v[22:23]
	v_pk_add_f32 v[120:121], v[120:121], v[24:25]
	v_pk_mul_f32 v[118:119], v[118:119], s[34:35] op_sel_hi:[1,0]
	v_pk_mul_f32 v[120:121], v[120:121], s[34:35] op_sel_hi:[1,0]
	global_store_dwordx4 v[130:131], v[118:121], off offset:64 nt
	v_pk_add_f32 v[114:115], v[114:115], v[18:19]
	v_pk_add_f32 v[116:117], v[116:117], v[20:21]
	v_pk_mul_f32 v[114:115], v[114:115], s[34:35] op_sel_hi:[1,0]
	v_pk_mul_f32 v[116:117], v[116:117], s[34:35] op_sel_hi:[1,0]
	global_store_dwordx4 v[132:133], v[114:117], off offset:64 nt
	v_pk_add_f32 v[110:111], v[110:111], v[14:15]
	v_pk_add_f32 v[112:113], v[112:113], v[16:17]
	v_pk_mul_f32 v[110:111], v[110:111], s[34:35] op_sel_hi:[1,0]
	v_pk_mul_f32 v[112:113], v[112:113], s[34:35] op_sel_hi:[1,0]
	global_store_dwordx4 v[130:131], v[110:113], off offset:128 nt
	v_pk_add_f32 v[106:107], v[106:107], v[10:11]
	v_pk_add_f32 v[108:109], v[108:109], v[12:13]
	v_pk_mul_f32 v[106:107], v[106:107], s[34:35] op_sel_hi:[1,0]
	v_pk_mul_f32 v[108:109], v[108:109], s[34:35] op_sel_hi:[1,0]
	global_store_dwordx4 v[132:133], v[106:109], off offset:128 nt
	v_pk_add_f32 v[102:103], v[102:103], v[6:7]
	v_pk_add_f32 v[104:105], v[104:105], v[8:9]
	v_pk_mul_f32 v[102:103], v[102:103], s[34:35] op_sel_hi:[1,0]
	v_pk_mul_f32 v[104:105], v[104:105], s[34:35] op_sel_hi:[1,0]
	global_store_dwordx4 v[130:131], v[102:105], off offset:192 nt
	v_pk_add_f32 v[98:99], v[98:99], v[2:3]
	v_pk_add_f32 v[100:101], v[100:101], v[4:5]
	v_pk_mul_f32 v[98:99], v[98:99], s[34:35] op_sel_hi:[1,0]
	v_pk_mul_f32 v[100:101], v[100:101], s[34:35] op_sel_hi:[1,0]
	global_store_dwordx4 v[132:133], v[98:101], off offset:192 nt
	s_endpgm
	.p2alignl 8, 3212836864
